# reversed phase of the per-tile alternating s_setprio (waves 0-3 prioritised in the first tile of a barrier block)
# speedup vs baseline: 1.0031x; 1.0031x over previous
.LBB0_734:
	s_cmp_eq_u32 s100, 1
	s_cbranch_scc1 .Lattn_pa0
	s_setprio 1
	s_branch .Lattn_pb0

.Lattn_pb0:
	s_waitcnt lgkmcnt(6)
	v_mfma_f32_16x16x32_bf16 v[64:67], v[160:163], v[96:99], 0
	v_exp_f32_e32 v88, v88
	v_mfma_f32_16x16x32_bf16 v[68:71], v[160:163], v[112:115], 0
	v_exp_f32_e32 v92, v92
	ds_read_b128 v[234:237], v209 offset:6144
	s_add_u32 s16, s22, s10
	s_addc_u32 s17, s23, s11
	s_add_u32 s15, s22, s12
	s_addc_u32 s14, s23, s13
	s_add_u32 s8, s16, 0x3bc00200
	s_addc_u32 s9, s17, 0
	s_add_u32 s6, s15, 0x23a50000
	s_addc_u32 s7, s14, 0
	s_waitcnt lgkmcnt(6)
	v_mfma_f32_16x16x32_bf16 v[0:3], v[164:167], v[216:219], v[0:3]
	v_cvt_pk_bf16_f32 v242, v80, v81
	v_mfma_f32_16x16x32_bf16 v[4:7], v[164:167], v[238:241], v[4:7]
	v_exp_f32_e32 v89, v89
	ds_read_b128 v[160:163], v201 offset:20480
	s_waitcnt vmcnt(4)
	ds_write_b128 v225, v[152:155] offset:49152
	s_waitcnt lgkmcnt(7)
	v_mfma_f32_16x16x32_bf16 v[68:71], v[168:171], v[116:119], v[68:71]
	v_exp_f32_e32 v93, v93
	v_mfma_f32_16x16x32_bf16 v[64:67], v[168:171], v[100:103], v[64:67]
	v_cvt_pk_bf16_f32 v243, v82, v83
	ds_read_b128 v[164:167], v209 offset:8192
	ds_write_b128 v226, v[156:159] offset:49152
	s_waitcnt lgkmcnt(8)
	v_mfma_f32_16x16x32_bf16 v[12:15], v[172:175], v[238:241], v[12:15]
	v_exp_f32_e32 v90, v90
	v_mfma_f32_16x16x32_bf16 v[8:11], v[172:175], v[216:219], v[8:11]
	v_exp_f32_e32 v94, v94
	ds_read_b128 v[168:171], v202 offset:20480
	ds_write_b64 v227, v[132:133] offset:32768
	s_waitcnt lgkmcnt(9)
	v_mfma_f32_16x16x32_bf16 v[64:67], v[176:179], v[104:107], v[64:67]
	v_cvt_pk_bf16_f32 v204, v84, v85
	v_mfma_f32_16x16x32_bf16 v[68:71], v[176:179], v[120:123], v[68:71]
	v_exp_f32_e32 v91, v91
	ds_read_b128 v[172:175], v209 offset:10240
	ds_write_b64 v228, v[134:135] offset:32768
	s_waitcnt lgkmcnt(10)
	v_mfma_f32_16x16x32_bf16 v[16:19], v[180:183], v[216:219], v[16:19]
	v_exp_f32_e32 v95, v95
	v_mfma_f32_16x16x32_bf16 v[20:23], v[180:183], v[238:241], v[20:23]
	v_cvt_pk_bf16_f32 v205, v86, v87
	v_add_f32_e32 v220, v220, v88
	ds_read_b128 v[176:179], v203 offset:20480
	ds_write_b64 v229, v[128:129] offset:32768
	s_waitcnt lgkmcnt(11)
	v_mfma_f32_16x16x32_bf16 v[68:71], v[230:233], v[124:127], v[68:71]
	v_add_f32_e32 v221, v221, v92
	v_add_f32_e32 v220, v220, v89
	v_mfma_f32_16x16x32_bf16 v[64:67], v[230:233], v[108:111], v[64:67]
	v_add_f32_e32 v221, v221, v93
	v_cvt_pk_bf16_f32 v244, v88, v89
	ds_read_b128 v[180:183], v209 offset:12288
	ds_write_b64 v184, v[130:131] offset:32768
	s_waitcnt lgkmcnt(12)
	v_mfma_f32_16x16x32_bf16 v[28:31], v[234:237], v[238:241], v[28:31]
	v_cvt_pk_bf16_f32 v245, v90, v91
	v_cvt_pk_bf16_f32 v206, v92, v93
	v_mfma_f32_16x16x32_bf16 v[24:27], v[234:237], v[216:219], v[24:27]
	v_cvt_pk_bf16_f32 v207, v94, v95
	ds_read_b128 v[230:233], v246 offset:20480
	global_load_dwordx4 v[132:135], v198, s[8:9]
	s_waitcnt lgkmcnt(12)
	v_mfma_f32_16x16x32_bf16 v[72:75], v[160:163], v[96:99], 0
	v_add_f32_e32 v220, v220, v90
	v_add_f32_e32 v221, v221, v94
	v_mfma_f32_16x16x32_bf16 v[76:79], v[160:163], v[112:115], 0
	v_add_f32_e32 v220, v220, v91
	v_add_f32_e32 v221, v221, v95
	ds_read_b128 v[234:237], v209 offset:14336
	global_load_dwordx4 v[128:131], v199, s[8:9]
	s_waitcnt lgkmcnt(11)
	v_mfma_f32_16x16x32_bf16 v[32:35], v[164:167], v[216:219], v[32:35]
	v_add_f32_e32 v194, v194, v220
	v_add_f32_e32 v195, v195, v221
	v_mfma_f32_16x16x32_bf16 v[36:39], v[164:167], v[238:241], v[36:39]
	v_exp_f32_e32 v64, v64
	ds_read_b128 v[160:163], v201 offset:24576
	global_load_dwordx4 v[152:155], v196, s[6:7]
	s_waitcnt lgkmcnt(10)
	v_mfma_f32_16x16x32_bf16 v[76:79], v[168:171], v[116:119], v[76:79]
	v_exp_f32_e32 v68, v68
	v_mfma_f32_16x16x32_bf16 v[72:75], v[168:171], v[100:103], v[72:75]
	v_exp_f32_e32 v65, v65
	ds_read_b128 v[164:167], v210 offset:0
	global_load_dwordx4 v[156:159], v197, s[6:7]
	s_waitcnt lgkmcnt(9)
	v_mfma_f32_16x16x32_bf16 v[44:47], v[172:175], v[238:241], v[44:47]
	v_exp_f32_e32 v69, v69
	v_mfma_f32_16x16x32_bf16 v[40:43], v[172:175], v[216:219], v[40:43]
	v_exp_f32_e32 v66, v66
	ds_read_b128 v[168:171], v202 offset:24576
	s_waitcnt lgkmcnt(8)
	v_mfma_f32_16x16x32_bf16 v[72:75], v[176:179], v[104:107], v[72:75]
	v_exp_f32_e32 v70, v70
	v_mfma_f32_16x16x32_bf16 v[76:79], v[176:179], v[120:123], v[76:79]
	v_exp_f32_e32 v67, v67
	ds_read_b128 v[172:175], v210 offset:2048
	s_waitcnt lgkmcnt(7)
	v_mfma_f32_16x16x32_bf16 v[48:51], v[180:183], v[216:219], v[48:51]
	v_exp_f32_e32 v71, v71
	v_mfma_f32_16x16x32_bf16 v[52:55], v[180:183], v[238:241], v[52:55]
	v_add_f32_e32 v220, v64, v65
	ds_read_b128 v[176:179], v203 offset:24576
	s_waitcnt lgkmcnt(6)
	v_mfma_f32_16x16x32_bf16 v[76:79], v[230:233], v[124:127], v[76:79]
	v_add_f32_e32 v221, v68, v69
	v_mfma_f32_16x16x32_bf16 v[72:75], v[230:233], v[108:111], v[72:75]
	v_add_f32_e32 v220, v220, v66
	ds_read_b128 v[180:183], v210 offset:4096
	s_waitcnt lgkmcnt(6)
	v_mfma_f32_16x16x32_bf16 v[60:63], v[234:237], v[238:241], v[60:63]
	v_add_f32_e32 v221, v221, v70
	v_add_f32_e32 v220, v220, v67
	v_mfma_f32_16x16x32_bf16 v[56:59], v[234:237], v[216:219], v[56:59]
	v_add_f32_e32 v221, v221, v71
	ds_read_b128 v[230:233], v246 offset:24576
	s_waitcnt lgkmcnt(6)
	v_mfma_f32_16x16x32_bf16 v[80:83], v[160:163], v[96:99], 0
	v_exp_f32_e32 v72, v72
	v_mfma_f32_16x16x32_bf16 v[84:87], v[160:163], v[112:115], 0
	v_exp_f32_e32 v76, v76
	ds_read_b128 v[234:237], v210 offset:6144
	s_waitcnt lgkmcnt(6)
	v_mfma_f32_16x16x32_bf16 v[0:3], v[164:167], v[242:245], v[0:3]
	v_exp_f32_e32 v73, v73
	v_mfma_f32_16x16x32_bf16 v[4:7], v[164:167], v[204:207], v[4:7]
	v_exp_f32_e32 v77, v77
	ds_read_b128 v[160:163], v201 offset:28672
	s_waitcnt lgkmcnt(6)
	v_mfma_f32_16x16x32_bf16 v[84:87], v[168:171], v[116:119], v[84:87]
	v_exp_f32_e32 v74, v74
	v_mfma_f32_16x16x32_bf16 v[80:83], v[168:171], v[100:103], v[80:83]
	v_exp_f32_e32 v78, v78
	ds_read_b128 v[164:167], v210 offset:8192
	s_waitcnt lgkmcnt(6)
	v_mfma_f32_16x16x32_bf16 v[12:15], v[172:175], v[204:207], v[12:15]
	v_exp_f32_e32 v75, v75
	v_mfma_f32_16x16x32_bf16 v[8:11], v[172:175], v[242:245], v[8:11]
	v_exp_f32_e32 v79, v79
	ds_read_b128 v[168:171], v202 offset:28672
	s_waitcnt lgkmcnt(6)
	v_mfma_f32_16x16x32_bf16 v[80:83], v[176:179], v[104:107], v[80:83]
	v_add_f32_e32 v220, v220, v72
	v_add_f32_e32 v221, v221, v76
	v_mfma_f32_16x16x32_bf16 v[84:87], v[176:179], v[120:123], v[84:87]
	v_add_f32_e32 v220, v220, v73
	ds_read_b128 v[172:175], v210 offset:10240
	s_waitcnt lgkmcnt(6)
	v_mfma_f32_16x16x32_bf16 v[16:19], v[180:183], v[242:245], v[16:19]
	v_add_f32_e32 v221, v221, v77
	v_add_f32_e32 v220, v220, v74
	v_mfma_f32_16x16x32_bf16 v[20:23], v[180:183], v[204:207], v[20:23]
	v_add_f32_e32 v221, v221, v78
	ds_read_b128 v[176:179], v203 offset:28672
	s_waitcnt lgkmcnt(6)
	v_mfma_f32_16x16x32_bf16 v[84:87], v[230:233], v[124:127], v[84:87]
	v_add_f32_e32 v220, v220, v75
	v_add_f32_e32 v221, v221, v79
	v_mfma_f32_16x16x32_bf16 v[80:83], v[230:233], v[108:111], v[80:83]
	v_cvt_pk_bf16_f32 v216, v64, v65
	ds_read_b128 v[180:183], v210 offset:12288
	s_waitcnt lgkmcnt(6)
	v_mfma_f32_16x16x32_bf16 v[28:31], v[234:237], v[204:207], v[28:31]
	v_cvt_pk_bf16_f32 v217, v66, v67
	v_cvt_pk_bf16_f32 v238, v68, v69
	v_mfma_f32_16x16x32_bf16 v[24:27], v[234:237], v[242:245], v[24:27]
	v_cvt_pk_bf16_f32 v239, v70, v71
	ds_read_b128 v[230:233], v246 offset:28672
	s_waitcnt lgkmcnt(6)
	v_mfma_f32_16x16x32_bf16 v[88:91], v[160:163], v[96:99], 0
	v_exp_f32_e32 v80, v80
	v_mfma_f32_16x16x32_bf16 v[92:95], v[160:163], v[112:115], 0
	v_exp_f32_e32 v84, v84
	ds_read_b128 v[234:237], v210 offset:14336
	s_waitcnt lgkmcnt(6)
	v_mfma_f32_16x16x32_bf16 v[32:35], v[164:167], v[242:245], v[32:35]
	v_exp_f32_e32 v81, v81
	v_mfma_f32_16x16x32_bf16 v[36:39], v[164:167], v[204:207], v[36:39]
	v_exp_f32_e32 v85, v85
	ds_read_b128 v[160:163], v201 offset:32768
	s_waitcnt lgkmcnt(6)
	v_mfma_f32_16x16x32_bf16 v[92:95], v[168:171], v[116:119], v[92:95]
	v_exp_f32_e32 v82, v82
	v_mfma_f32_16x16x32_bf16 v[88:91], v[168:171], v[100:103], v[88:91]
	v_exp_f32_e32 v86, v86
	ds_read_b128 v[164:167], v209 offset:16384
	s_waitcnt lgkmcnt(6)
	v_mfma_f32_16x16x32_bf16 v[44:47], v[172:175], v[204:207], v[44:47]
	v_exp_f32_e32 v83, v83
	v_mfma_f32_16x16x32_bf16 v[40:43], v[172:175], v[242:245], v[40:43]
	v_exp_f32_e32 v87, v87
	ds_read_b128 v[168:171], v202 offset:32768
	s_waitcnt lgkmcnt(6)
	v_mfma_f32_16x16x32_bf16 v[88:91], v[176:179], v[104:107], v[88:91]
	v_add_f32_e32 v220, v220, v80
	v_add_f32_e32 v221, v221, v84
	v_mfma_f32_16x16x32_bf16 v[92:95], v[176:179], v[120:123], v[92:95]
	v_add_f32_e32 v220, v220, v81
	ds_read_b128 v[172:175], v209 offset:18432
	s_waitcnt lgkmcnt(6)
	v_mfma_f32_16x16x32_bf16 v[48:51], v[180:183], v[242:245], v[48:51]
	v_add_f32_e32 v221, v221, v85
	v_add_f32_e32 v220, v220, v82
	v_mfma_f32_16x16x32_bf16 v[52:55], v[180:183], v[204:207], v[52:55]
	v_add_f32_e32 v221, v221, v86
	ds_read_b128 v[176:179], v203 offset:32768
	s_waitcnt lgkmcnt(6)
	v_mfma_f32_16x16x32_bf16 v[92:95], v[230:233], v[124:127], v[92:95]
	v_add_f32_e32 v220, v220, v83
	v_add_f32_e32 v221, v221, v87
	v_mfma_f32_16x16x32_bf16 v[88:91], v[230:233], v[108:111], v[88:91]
	v_cvt_pk_bf16_f32 v218, v72, v73
	ds_read_b128 v[180:183], v209 offset:20480
	s_waitcnt lgkmcnt(6)
	v_mfma_f32_16x16x32_bf16 v[60:63], v[234:237], v[204:207], v[60:63]
	v_cvt_pk_bf16_f32 v219, v74, v75
	v_cvt_pk_bf16_f32 v240, v76, v77
	v_mfma_f32_16x16x32_bf16 v[56:59], v[234:237], v[242:245], v[56:59]
	v_cvt_pk_bf16_f32 v241, v78, v79
	ds_read_b128 v[230:233], v246 offset:32768
	s_cmp_eq_u32 s100, 0
	s_cbranch_scc1 .Lattn_pa1
	s_setprio 1
	s_branch .Lattn_pb1

.Lattn_pb1:
	s_waitcnt lgkmcnt(6)
	v_mfma_f32_16x16x32_bf16 v[64:67], v[160:163], v[96:99], 0
	v_exp_f32_e32 v88, v88
	v_mfma_f32_16x16x32_bf16 v[68:71], v[160:163], v[112:115], 0
	v_exp_f32_e32 v92, v92
	ds_read_b128 v[234:237], v209 offset:22528
	s_add_u32 s8, s16, 0x3bc00280
	s_addc_u32 s9, s17, 0
	s_add_u32 s6, s15, 0x23a60000
	s_addc_u32 s7, s14, 0
	s_waitcnt lgkmcnt(6)
	v_mfma_f32_16x16x32_bf16 v[0:3], v[164:167], v[216:219], v[0:3]
	v_cvt_pk_bf16_f32 v242, v80, v81
	v_mfma_f32_16x16x32_bf16 v[4:7], v[164:167], v[238:241], v[4:7]
	v_exp_f32_e32 v89, v89
	ds_read_b128 v[160:163], v201 offset:36864
	s_waitcnt vmcnt(4)
	ds_write_b128 v225, v[136:139] offset:0
	s_waitcnt lgkmcnt(7)
	v_mfma_f32_16x16x32_bf16 v[68:71], v[168:171], v[116:119], v[68:71]
	v_exp_f32_e32 v93, v93
	v_mfma_f32_16x16x32_bf16 v[64:67], v[168:171], v[100:103], v[64:67]
	v_cvt_pk_bf16_f32 v243, v82, v83
	ds_read_b128 v[164:167], v209 offset:24576
	ds_write_b128 v226, v[140:143] offset:0
	s_waitcnt lgkmcnt(8)
	v_mfma_f32_16x16x32_bf16 v[12:15], v[172:175], v[238:241], v[12:15]
	v_exp_f32_e32 v90, v90
	v_mfma_f32_16x16x32_bf16 v[8:11], v[172:175], v[216:219], v[8:11]
	v_exp_f32_e32 v94, v94
	ds_read_b128 v[168:171], v202 offset:36864
	ds_write_b64 v227, v[148:149] offset:49152
	s_waitcnt lgkmcnt(9)
	v_mfma_f32_16x16x32_bf16 v[64:67], v[176:179], v[104:107], v[64:67]
	v_cvt_pk_bf16_f32 v204, v84, v85
	v_mfma_f32_16x16x32_bf16 v[68:71], v[176:179], v[120:123], v[68:71]
	v_exp_f32_e32 v91, v91
	ds_read_b128 v[172:175], v209 offset:26624
	ds_write_b64 v228, v[150:151] offset:49152
	s_waitcnt lgkmcnt(10)
	v_mfma_f32_16x16x32_bf16 v[16:19], v[180:183], v[216:219], v[16:19]
	v_exp_f32_e32 v95, v95
	v_mfma_f32_16x16x32_bf16 v[20:23], v[180:183], v[238:241], v[20:23]
	v_cvt_pk_bf16_f32 v205, v86, v87
	v_add_f32_e32 v220, v220, v88
	ds_read_b128 v[176:179], v203 offset:36864
	ds_write_b64 v229, v[144:145] offset:49152
	s_waitcnt lgkmcnt(11)
	v_mfma_f32_16x16x32_bf16 v[68:71], v[230:233], v[124:127], v[68:71]
	v_add_f32_e32 v221, v221, v92
	v_add_f32_e32 v220, v220, v89
	v_mfma_f32_16x16x32_bf16 v[64:67], v[230:233], v[108:111], v[64:67]
	v_add_f32_e32 v221, v221, v93
	v_cvt_pk_bf16_f32 v244, v88, v89
	ds_read_b128 v[180:183], v209 offset:28672
	ds_write_b64 v184, v[146:147] offset:49152
	s_waitcnt lgkmcnt(12)
	v_mfma_f32_16x16x32_bf16 v[28:31], v[234:237], v[238:241], v[28:31]
	v_cvt_pk_bf16_f32 v245, v90, v91
	v_cvt_pk_bf16_f32 v206, v92, v93
	v_mfma_f32_16x16x32_bf16 v[24:27], v[234:237], v[216:219], v[24:27]
	v_cvt_pk_bf16_f32 v207, v94, v95
	ds_read_b128 v[230:233], v246 offset:36864
	global_load_dwordx4 v[148:151], v198, s[8:9]
	s_waitcnt lgkmcnt(12)
	v_mfma_f32_16x16x32_bf16 v[72:75], v[160:163], v[96:99], 0
	v_add_f32_e32 v220, v220, v90
	v_add_f32_e32 v221, v221, v94
	v_mfma_f32_16x16x32_bf16 v[76:79], v[160:163], v[112:115], 0
	v_add_f32_e32 v220, v220, v91
	v_add_f32_e32 v221, v221, v95
	ds_read_b128 v[234:237], v209 offset:30720
	global_load_dwordx4 v[144:147], v199, s[8:9]
	s_waitcnt lgkmcnt(11)
	v_mfma_f32_16x16x32_bf16 v[32:35], v[164:167], v[216:219], v[32:35]
	v_add_f32_e32 v194, v194, v220
	v_add_f32_e32 v195, v195, v221
	v_mfma_f32_16x16x32_bf16 v[36:39], v[164:167], v[238:241], v[36:39]
	v_exp_f32_e32 v64, v64
	ds_read_b128 v[160:163], v201 offset:40960
	global_load_dwordx4 v[136:139], v196, s[6:7]
	s_waitcnt lgkmcnt(10)
	v_mfma_f32_16x16x32_bf16 v[76:79], v[168:171], v[116:119], v[76:79]
	v_exp_f32_e32 v68, v68
	v_mfma_f32_16x16x32_bf16 v[72:75], v[168:171], v[100:103], v[72:75]
	v_exp_f32_e32 v65, v65
	ds_read_b128 v[164:167], v210 offset:16384
	global_load_dwordx4 v[140:143], v197, s[6:7]
	s_waitcnt lgkmcnt(9)
	v_mfma_f32_16x16x32_bf16 v[44:47], v[172:175], v[238:241], v[44:47]
	v_exp_f32_e32 v69, v69
	v_mfma_f32_16x16x32_bf16 v[40:43], v[172:175], v[216:219], v[40:43]
	v_exp_f32_e32 v66, v66
	ds_read_b128 v[168:171], v202 offset:40960
	s_waitcnt lgkmcnt(8)
	v_mfma_f32_16x16x32_bf16 v[72:75], v[176:179], v[104:107], v[72:75]
	v_exp_f32_e32 v70, v70
	v_mfma_f32_16x16x32_bf16 v[76:79], v[176:179], v[120:123], v[76:79]
	v_exp_f32_e32 v67, v67
	ds_read_b128 v[172:175], v210 offset:18432
	s_waitcnt lgkmcnt(7)
	v_mfma_f32_16x16x32_bf16 v[48:51], v[180:183], v[216:219], v[48:51]
	v_exp_f32_e32 v71, v71
	v_mfma_f32_16x16x32_bf16 v[52:55], v[180:183], v[238:241], v[52:55]
	v_add_f32_e32 v220, v64, v65
	ds_read_b128 v[176:179], v203 offset:40960
	s_waitcnt lgkmcnt(6)
	v_mfma_f32_16x16x32_bf16 v[76:79], v[230:233], v[124:127], v[76:79]
	v_add_f32_e32 v221, v68, v69
	v_mfma_f32_16x16x32_bf16 v[72:75], v[230:233], v[108:111], v[72:75]
	v_add_f32_e32 v220, v220, v66
	ds_read_b128 v[180:183], v210 offset:20480
	s_waitcnt lgkmcnt(6)
	v_mfma_f32_16x16x32_bf16 v[60:63], v[234:237], v[238:241], v[60:63]
	v_add_f32_e32 v221, v221, v70
	v_add_f32_e32 v220, v220, v67
	v_mfma_f32_16x16x32_bf16 v[56:59], v[234:237], v[216:219], v[56:59]
	v_add_f32_e32 v221, v221, v71
	ds_read_b128 v[230:233], v246 offset:40960
	s_waitcnt lgkmcnt(6)
	v_mfma_f32_16x16x32_bf16 v[80:83], v[160:163], v[96:99], 0
	v_exp_f32_e32 v72, v72
	v_mfma_f32_16x16x32_bf16 v[84:87], v[160:163], v[112:115], 0
	v_exp_f32_e32 v76, v76
	ds_read_b128 v[234:237], v210 offset:22528
	s_waitcnt lgkmcnt(6)
	v_mfma_f32_16x16x32_bf16 v[0:3], v[164:167], v[242:245], v[0:3]
	v_exp_f32_e32 v73, v73
	v_mfma_f32_16x16x32_bf16 v[4:7], v[164:167], v[204:207], v[4:7]
	v_exp_f32_e32 v77, v77
	ds_read_b128 v[160:163], v201 offset:45056
	s_waitcnt lgkmcnt(6)
	v_mfma_f32_16x16x32_bf16 v[84:87], v[168:171], v[116:119], v[84:87]
	v_exp_f32_e32 v74, v74
	v_mfma_f32_16x16x32_bf16 v[80:83], v[168:171], v[100:103], v[80:83]
	v_exp_f32_e32 v78, v78
	ds_read_b128 v[164:167], v210 offset:24576
	s_waitcnt lgkmcnt(6)
	v_mfma_f32_16x16x32_bf16 v[12:15], v[172:175], v[204:207], v[12:15]
	v_exp_f32_e32 v75, v75
	v_mfma_f32_16x16x32_bf16 v[8:11], v[172:175], v[242:245], v[8:11]
	v_exp_f32_e32 v79, v79
	ds_read_b128 v[168:171], v202 offset:45056
	s_waitcnt lgkmcnt(6)
	v_mfma_f32_16x16x32_bf16 v[80:83], v[176:179], v[104:107], v[80:83]
	v_add_f32_e32 v220, v220, v72
	v_add_f32_e32 v221, v221, v76
	v_mfma_f32_16x16x32_bf16 v[84:87], v[176:179], v[120:123], v[84:87]
	v_add_f32_e32 v220, v220, v73
	ds_read_b128 v[172:175], v210 offset:26624
	s_waitcnt lgkmcnt(6)
	v_mfma_f32_16x16x32_bf16 v[16:19], v[180:183], v[242:245], v[16:19]
	v_add_f32_e32 v221, v221, v77
	v_add_f32_e32 v220, v220, v74
	v_mfma_f32_16x16x32_bf16 v[20:23], v[180:183], v[204:207], v[20:23]
	v_add_f32_e32 v221, v221, v78
	ds_read_b128 v[176:179], v203 offset:45056
	s_waitcnt lgkmcnt(6)
	v_mfma_f32_16x16x32_bf16 v[84:87], v[230:233], v[124:127], v[84:87]
	v_add_f32_e32 v220, v220, v75
	v_add_f32_e32 v221, v221, v79
	v_mfma_f32_16x16x32_bf16 v[80:83], v[230:233], v[108:111], v[80:83]
	v_cvt_pk_bf16_f32 v216, v64, v65
	ds_read_b128 v[180:183], v210 offset:28672
	s_waitcnt lgkmcnt(6)
	v_mfma_f32_16x16x32_bf16 v[28:31], v[234:237], v[204:207], v[28:31]
	v_cvt_pk_bf16_f32 v217, v66, v67
	v_cvt_pk_bf16_f32 v238, v68, v69
	v_mfma_f32_16x16x32_bf16 v[24:27], v[234:237], v[242:245], v[24:27]
	v_cvt_pk_bf16_f32 v239, v70, v71
	ds_read_b128 v[230:233], v246 offset:45056
	s_waitcnt lgkmcnt(6)
	v_mfma_f32_16x16x32_bf16 v[88:91], v[160:163], v[96:99], 0
	v_exp_f32_e32 v80, v80
	v_mfma_f32_16x16x32_bf16 v[92:95], v[160:163], v[112:115], 0
	v_exp_f32_e32 v84, v84
	ds_read_b128 v[234:237], v210 offset:30720
	s_waitcnt lgkmcnt(6)
	v_mfma_f32_16x16x32_bf16 v[32:35], v[164:167], v[242:245], v[32:35]
	v_exp_f32_e32 v81, v81
	v_mfma_f32_16x16x32_bf16 v[36:39], v[164:167], v[204:207], v[36:39]
	v_exp_f32_e32 v85, v85
	s_waitcnt lgkmcnt(5)
	v_mfma_f32_16x16x32_bf16 v[92:95], v[168:171], v[116:119], v[92:95]
	v_exp_f32_e32 v82, v82
	v_mfma_f32_16x16x32_bf16 v[88:91], v[168:171], v[100:103], v[88:91]
	v_exp_f32_e32 v86, v86
	s_waitcnt lgkmcnt(4)
	v_mfma_f32_16x16x32_bf16 v[44:47], v[172:175], v[204:207], v[44:47]
	v_exp_f32_e32 v83, v83
	v_mfma_f32_16x16x32_bf16 v[40:43], v[172:175], v[242:245], v[40:43]
	v_exp_f32_e32 v87, v87
	s_waitcnt lgkmcnt(3)
	v_mfma_f32_16x16x32_bf16 v[88:91], v[176:179], v[104:107], v[88:91]
	v_add_f32_e32 v220, v220, v80
	v_add_f32_e32 v221, v221, v84
	v_mfma_f32_16x16x32_bf16 v[92:95], v[176:179], v[120:123], v[92:95]
	v_add_f32_e32 v220, v220, v81
	s_waitcnt lgkmcnt(0)
	s_barrier
	ds_read_b128 v[160:163], v201 offset:49152
	ds_read_b128 v[164:167], v209 offset:32768
	ds_read_b128 v[168:171], v202 offset:49152
	ds_read_b128 v[172:175], v209 offset:34816
	v_mfma_f32_16x16x32_bf16 v[48:51], v[180:183], v[242:245], v[48:51]
	v_add_f32_e32 v221, v221, v85
	v_add_f32_e32 v220, v220, v82
	v_mfma_f32_16x16x32_bf16 v[52:55], v[180:183], v[204:207], v[52:55]
	v_add_f32_e32 v221, v221, v86
	ds_read_b128 v[176:179], v203 offset:49152
	v_mfma_f32_16x16x32_bf16 v[92:95], v[230:233], v[124:127], v[92:95]
	v_add_f32_e32 v220, v220, v83
	v_add_f32_e32 v221, v221, v87
	v_mfma_f32_16x16x32_bf16 v[88:91], v[230:233], v[108:111], v[88:91]
	v_cvt_pk_bf16_f32 v218, v72, v73
	ds_read_b128 v[180:183], v209 offset:36864
	v_mfma_f32_16x16x32_bf16 v[60:63], v[234:237], v[204:207], v[60:63]
	v_cvt_pk_bf16_f32 v219, v74, v75
	v_cvt_pk_bf16_f32 v240, v76, v77
	v_mfma_f32_16x16x32_bf16 v[56:59], v[234:237], v[242:245], v[56:59]
	v_cvt_pk_bf16_f32 v241, v78, v79
	ds_read_b128 v[230:233], v246 offset:49152
	s_cmp_eq_u32 s100, 1
	s_cbranch_scc1 .Lattn_pa2
	s_setprio 1
	s_branch .Lattn_pb2

.Lattn_pb2:
	s_waitcnt lgkmcnt(6)
	v_mfma_f32_16x16x32_bf16 v[64:67], v[160:163], v[96:99], 0
	v_exp_f32_e32 v88, v88
	v_mfma_f32_16x16x32_bf16 v[68:71], v[160:163], v[112:115], 0
	v_exp_f32_e32 v92, v92
	ds_read_b128 v[234:237], v209 offset:38912
	s_add_u32 s8, s16, 0x3bc00300
	s_addc_u32 s9, s17, 0
	s_add_u32 s6, s15, 0x23a70000
	s_addc_u32 s7, s14, 0
	s_waitcnt lgkmcnt(6)
	v_mfma_f32_16x16x32_bf16 v[0:3], v[164:167], v[216:219], v[0:3]
	v_cvt_pk_bf16_f32 v242, v80, v81
	v_mfma_f32_16x16x32_bf16 v[4:7], v[164:167], v[238:241], v[4:7]
	v_exp_f32_e32 v89, v89
	ds_read_b128 v[160:163], v201 offset:53248
	s_waitcnt vmcnt(4)
	ds_write_b128 v225, v[152:155] offset:16384
	s_waitcnt lgkmcnt(7)
	v_mfma_f32_16x16x32_bf16 v[68:71], v[168:171], v[116:119], v[68:71]
	v_exp_f32_e32 v93, v93
	v_mfma_f32_16x16x32_bf16 v[64:67], v[168:171], v[100:103], v[64:67]
	v_cvt_pk_bf16_f32 v243, v82, v83
	ds_read_b128 v[164:167], v209 offset:40960
	ds_write_b128 v226, v[156:159] offset:16384
	s_waitcnt lgkmcnt(8)
	v_mfma_f32_16x16x32_bf16 v[12:15], v[172:175], v[238:241], v[12:15]
	v_exp_f32_e32 v90, v90
	v_mfma_f32_16x16x32_bf16 v[8:11], v[172:175], v[216:219], v[8:11]
	v_exp_f32_e32 v94, v94
	ds_read_b128 v[168:171], v202 offset:53248
	ds_write_b64 v227, v[132:133] offset:0
	s_waitcnt lgkmcnt(9)
	v_mfma_f32_16x16x32_bf16 v[64:67], v[176:179], v[104:107], v[64:67]
	v_cvt_pk_bf16_f32 v204, v84, v85
	v_mfma_f32_16x16x32_bf16 v[68:71], v[176:179], v[120:123], v[68:71]
	v_exp_f32_e32 v91, v91
	ds_read_b128 v[172:175], v209 offset:43008
	ds_write_b64 v228, v[134:135] offset:0
	s_waitcnt lgkmcnt(10)
	v_mfma_f32_16x16x32_bf16 v[16:19], v[180:183], v[216:219], v[16:19]
	v_exp_f32_e32 v95, v95
	v_mfma_f32_16x16x32_bf16 v[20:23], v[180:183], v[238:241], v[20:23]
	v_cvt_pk_bf16_f32 v205, v86, v87
	v_add_f32_e32 v220, v220, v88
	ds_read_b128 v[176:179], v203 offset:53248
	ds_write_b64 v229, v[128:129] offset:0
	s_waitcnt lgkmcnt(11)
	v_mfma_f32_16x16x32_bf16 v[68:71], v[230:233], v[124:127], v[68:71]
	v_add_f32_e32 v221, v221, v92
	v_add_f32_e32 v220, v220, v89
	v_mfma_f32_16x16x32_bf16 v[64:67], v[230:233], v[108:111], v[64:67]
	v_add_f32_e32 v221, v221, v93
	v_cvt_pk_bf16_f32 v244, v88, v89
	ds_read_b128 v[180:183], v209 offset:45056
	ds_write_b64 v184, v[130:131] offset:0
	s_waitcnt lgkmcnt(12)
	v_mfma_f32_16x16x32_bf16 v[28:31], v[234:237], v[238:241], v[28:31]
	v_cvt_pk_bf16_f32 v245, v90, v91
	v_cvt_pk_bf16_f32 v206, v92, v93
	v_mfma_f32_16x16x32_bf16 v[24:27], v[234:237], v[216:219], v[24:27]
	v_cvt_pk_bf16_f32 v207, v94, v95
	ds_read_b128 v[230:233], v246 offset:53248
	global_load_dwordx4 v[132:135], v198, s[8:9]
	s_waitcnt lgkmcnt(12)
	v_mfma_f32_16x16x32_bf16 v[72:75], v[160:163], v[96:99], 0
	v_add_f32_e32 v220, v220, v90
	v_add_f32_e32 v221, v221, v94
	v_mfma_f32_16x16x32_bf16 v[76:79], v[160:163], v[112:115], 0
	v_add_f32_e32 v220, v220, v91
	v_add_f32_e32 v221, v221, v95
	ds_read_b128 v[234:237], v209 offset:47104
	global_load_dwordx4 v[128:131], v199, s[8:9]
	s_waitcnt lgkmcnt(11)
	v_mfma_f32_16x16x32_bf16 v[32:35], v[164:167], v[216:219], v[32:35]
	v_add_f32_e32 v194, v194, v220
	v_add_f32_e32 v195, v195, v221
	v_mfma_f32_16x16x32_bf16 v[36:39], v[164:167], v[238:241], v[36:39]
	v_exp_f32_e32 v64, v64
	ds_read_b128 v[160:163], v201 offset:57344
	global_load_dwordx4 v[152:155], v196, s[6:7]
	s_waitcnt lgkmcnt(10)
	v_mfma_f32_16x16x32_bf16 v[76:79], v[168:171], v[116:119], v[76:79]
	v_exp_f32_e32 v68, v68
	v_mfma_f32_16x16x32_bf16 v[72:75], v[168:171], v[100:103], v[72:75]
	v_exp_f32_e32 v65, v65
	ds_read_b128 v[164:167], v210 offset:32768
	global_load_dwordx4 v[156:159], v197, s[6:7]
	s_waitcnt lgkmcnt(9)
	v_mfma_f32_16x16x32_bf16 v[44:47], v[172:175], v[238:241], v[44:47]
	v_exp_f32_e32 v69, v69
	v_mfma_f32_16x16x32_bf16 v[40:43], v[172:175], v[216:219], v[40:43]
	v_exp_f32_e32 v66, v66
	ds_read_b128 v[168:171], v202 offset:57344
	s_waitcnt lgkmcnt(8)
	v_mfma_f32_16x16x32_bf16 v[72:75], v[176:179], v[104:107], v[72:75]
	v_exp_f32_e32 v70, v70
	v_mfma_f32_16x16x32_bf16 v[76:79], v[176:179], v[120:123], v[76:79]
	v_exp_f32_e32 v67, v67
	ds_read_b128 v[172:175], v210 offset:34816
	s_waitcnt lgkmcnt(7)
	v_mfma_f32_16x16x32_bf16 v[48:51], v[180:183], v[216:219], v[48:51]
	v_exp_f32_e32 v71, v71
	v_mfma_f32_16x16x32_bf16 v[52:55], v[180:183], v[238:241], v[52:55]
	v_add_f32_e32 v220, v64, v65
	ds_read_b128 v[176:179], v203 offset:57344
	s_waitcnt lgkmcnt(6)
	v_mfma_f32_16x16x32_bf16 v[76:79], v[230:233], v[124:127], v[76:79]
	v_add_f32_e32 v221, v68, v69
	v_mfma_f32_16x16x32_bf16 v[72:75], v[230:233], v[108:111], v[72:75]
	v_add_f32_e32 v220, v220, v66
	ds_read_b128 v[180:183], v210 offset:36864
	s_waitcnt lgkmcnt(6)
	v_mfma_f32_16x16x32_bf16 v[60:63], v[234:237], v[238:241], v[60:63]
	v_add_f32_e32 v221, v221, v70
	v_add_f32_e32 v220, v220, v67
	v_mfma_f32_16x16x32_bf16 v[56:59], v[234:237], v[216:219], v[56:59]
	v_add_f32_e32 v221, v221, v71
	ds_read_b128 v[230:233], v246 offset:57344
	s_waitcnt lgkmcnt(6)
	v_mfma_f32_16x16x32_bf16 v[80:83], v[160:163], v[96:99], 0
	v_exp_f32_e32 v72, v72
	v_mfma_f32_16x16x32_bf16 v[84:87], v[160:163], v[112:115], 0
	v_exp_f32_e32 v76, v76
	ds_read_b128 v[234:237], v210 offset:38912
	s_waitcnt lgkmcnt(6)
	v_mfma_f32_16x16x32_bf16 v[0:3], v[164:167], v[242:245], v[0:3]
	v_exp_f32_e32 v73, v73
	v_mfma_f32_16x16x32_bf16 v[4:7], v[164:167], v[204:207], v[4:7]
	v_exp_f32_e32 v77, v77
	ds_read_b128 v[160:163], v201 offset:61440
	s_waitcnt lgkmcnt(6)
	v_mfma_f32_16x16x32_bf16 v[84:87], v[168:171], v[116:119], v[84:87]
	v_exp_f32_e32 v74, v74
	v_mfma_f32_16x16x32_bf16 v[80:83], v[168:171], v[100:103], v[80:83]
	v_exp_f32_e32 v78, v78
	ds_read_b128 v[164:167], v210 offset:40960
	s_waitcnt lgkmcnt(6)
	v_mfma_f32_16x16x32_bf16 v[12:15], v[172:175], v[204:207], v[12:15]
	v_exp_f32_e32 v75, v75
	v_mfma_f32_16x16x32_bf16 v[8:11], v[172:175], v[242:245], v[8:11]
	v_exp_f32_e32 v79, v79
	ds_read_b128 v[168:171], v202 offset:61440
	s_waitcnt lgkmcnt(6)
	v_mfma_f32_16x16x32_bf16 v[80:83], v[176:179], v[104:107], v[80:83]
	v_add_f32_e32 v220, v220, v72
	v_add_f32_e32 v221, v221, v76
	v_mfma_f32_16x16x32_bf16 v[84:87], v[176:179], v[120:123], v[84:87]
	v_add_f32_e32 v220, v220, v73
	ds_read_b128 v[172:175], v210 offset:43008
	s_waitcnt lgkmcnt(6)
	v_mfma_f32_16x16x32_bf16 v[16:19], v[180:183], v[242:245], v[16:19]
	v_add_f32_e32 v221, v221, v77
	v_add_f32_e32 v220, v220, v74
	v_mfma_f32_16x16x32_bf16 v[20:23], v[180:183], v[204:207], v[20:23]
	v_add_f32_e32 v221, v221, v78
	ds_read_b128 v[176:179], v203 offset:61440
	s_waitcnt lgkmcnt(6)
	v_mfma_f32_16x16x32_bf16 v[84:87], v[230:233], v[124:127], v[84:87]
	v_add_f32_e32 v220, v220, v75
	v_add_f32_e32 v221, v221, v79
	v_mfma_f32_16x16x32_bf16 v[80:83], v[230:233], v[108:111], v[80:83]
	v_cvt_pk_bf16_f32 v216, v64, v65
	ds_read_b128 v[180:183], v210 offset:45056
	s_waitcnt lgkmcnt(6)
	v_mfma_f32_16x16x32_bf16 v[28:31], v[234:237], v[204:207], v[28:31]
	v_cvt_pk_bf16_f32 v217, v66, v67
	v_cvt_pk_bf16_f32 v238, v68, v69
	v_mfma_f32_16x16x32_bf16 v[24:27], v[234:237], v[242:245], v[24:27]
	v_cvt_pk_bf16_f32 v239, v70, v71
	ds_read_b128 v[230:233], v246 offset:61440
	s_waitcnt lgkmcnt(6)
	v_mfma_f32_16x16x32_bf16 v[88:91], v[160:163], v[96:99], 0
	v_exp_f32_e32 v80, v80
	v_mfma_f32_16x16x32_bf16 v[92:95], v[160:163], v[112:115], 0
	v_exp_f32_e32 v84, v84
	ds_read_b128 v[234:237], v210 offset:47104
	s_waitcnt lgkmcnt(6)
	v_mfma_f32_16x16x32_bf16 v[32:35], v[164:167], v[242:245], v[32:35]
	v_exp_f32_e32 v81, v81
	v_mfma_f32_16x16x32_bf16 v[36:39], v[164:167], v[204:207], v[36:39]
	v_exp_f32_e32 v85, v85
	ds_read_b128 v[160:163], v201 offset:0
	s_waitcnt lgkmcnt(6)
	v_mfma_f32_16x16x32_bf16 v[92:95], v[168:171], v[116:119], v[92:95]
	v_exp_f32_e32 v82, v82
	v_mfma_f32_16x16x32_bf16 v[88:91], v[168:171], v[100:103], v[88:91]
	v_exp_f32_e32 v86, v86
	ds_read_b128 v[164:167], v209 offset:49152
	s_waitcnt lgkmcnt(6)
	v_mfma_f32_16x16x32_bf16 v[44:47], v[172:175], v[204:207], v[44:47]
	v_exp_f32_e32 v83, v83
	v_mfma_f32_16x16x32_bf16 v[40:43], v[172:175], v[242:245], v[40:43]
	v_exp_f32_e32 v87, v87
	ds_read_b128 v[168:171], v202 offset:0
	s_waitcnt lgkmcnt(6)
	v_mfma_f32_16x16x32_bf16 v[88:91], v[176:179], v[104:107], v[88:91]
	v_add_f32_e32 v220, v220, v80
	v_add_f32_e32 v221, v221, v84
	v_mfma_f32_16x16x32_bf16 v[92:95], v[176:179], v[120:123], v[92:95]
	v_add_f32_e32 v220, v220, v81
	ds_read_b128 v[172:175], v209 offset:51200
	s_waitcnt lgkmcnt(6)
	v_mfma_f32_16x16x32_bf16 v[48:51], v[180:183], v[242:245], v[48:51]
	v_add_f32_e32 v221, v221, v85
	v_add_f32_e32 v220, v220, v82
	v_mfma_f32_16x16x32_bf16 v[52:55], v[180:183], v[204:207], v[52:55]
	v_add_f32_e32 v221, v221, v86
	ds_read_b128 v[176:179], v203 offset:0
	s_waitcnt lgkmcnt(6)
	v_mfma_f32_16x16x32_bf16 v[92:95], v[230:233], v[124:127], v[92:95]
	v_add_f32_e32 v220, v220, v83
	v_add_f32_e32 v221, v221, v87
	v_mfma_f32_16x16x32_bf16 v[88:91], v[230:233], v[108:111], v[88:91]
	v_cvt_pk_bf16_f32 v218, v72, v73
	ds_read_b128 v[180:183], v209 offset:53248
	s_waitcnt lgkmcnt(6)
	v_mfma_f32_16x16x32_bf16 v[60:63], v[234:237], v[204:207], v[60:63]
	v_cvt_pk_bf16_f32 v219, v74, v75
	v_cvt_pk_bf16_f32 v240, v76, v77
	v_mfma_f32_16x16x32_bf16 v[56:59], v[234:237], v[242:245], v[56:59]
	v_cvt_pk_bf16_f32 v241, v78, v79
	ds_read_b128 v[230:233], v246 offset:0
	s_cmp_eq_u32 s100, 0
	s_cbranch_scc1 .Lattn_pa3
	s_setprio 1
	s_branch .Lattn_pb3
